# baseline (speedup 1.0000x reference)
.Lq_dma_loop:
	s_lshl_b32 s40, s38, 10
	s_add_u32 s42, s36, s40
	s_addc_u32 s43, s37, 0
	s_add_i32 s41, s40, 69680
	v_lshl_add_u64 v[114:115], s[42:43], 0, v[116:117]
	s_mov_b32 m0, s41
	s_add_i32 s38, s38, 14
	global_load_lds_dwordx4 v[114:115], off
	s_cmp_lt_u32 s38, 91
	s_cbranch_scc1 .Lq_dma_loop

.LBB1_44:
	s_or_b64 exec, exec, s[10:11]
	s_waitcnt lgkmcnt(0)
	s_barrier
	s_mul_i32 s0, s2, 0xffffff3c
	s_add_i32 s0, s0, 0xc350
	s_min_i32 s28, s0, 0xc4
	v_lshrrev_b32_e32 v86, 6, v0
	s_mul_i32 s29, s2, 0xc4
	s_mov_b64 s[0:1], -1
	s_and_b64 vcc, exec, vcc
	s_cbranch_vccz .LBB1_119
	s_and_saveexec_b64 s[0:1], s[14:15]
	s_cbranch_execz .LBB1_46
	v_or_b32_e32 v7, 0x10000, v6
	ds_read_b32 v7, v7
	v_add_u32_e32 v6, 0x10820, v6
	s_waitcnt lgkmcnt(0)
	ds_write_b32 v6, v7
.LBB1_46:
	s_or_b64 exec, exec, s[0:1]
	s_mov_b64 s[0:1], -1
	s_waitcnt lgkmcnt(0)
	s_barrier
	s_and_saveexec_b64 s[0:1], s[4:5]
	s_cbranch_execz .LBB1_51
	s_mov_b64 s[4:5], exec
	v_mbcnt_lo_u32_b32 v6, s4, 0
	v_mbcnt_hi_u32_b32 v6, s5, v6
	v_cmp_eq_u32_e32 vcc, 0, v6
	s_and_saveexec_b64 s[2:3], vcc
	s_cbranch_execz .LBB1_50
	s_bcnt1_i32_b64 s4, s[4:5]
	v_mul_lo_u32 v7, v77, s4
	v_mov_b32_e32 v8, 0
	global_atomic_add v7, v8, v7, s[26:27] sc0

.LBB1_137:
	s_or_b64 exec, exec, s[6:7]
	v_readfirstlane_b32 s10, v0
	s_cmp_ge_i32 s10, s28
	s_mov_b64 s[6:7], -1
	s_cbranch_scc1 .LBB1_132
	s_add_i32 s8, s10, s29
	s_ashr_i32 s9, s8, 31
	s_cmp_lt_u32 s10, 182
	s_cbranch_scc0 .Lq_glob
	s_lshl_b32 s6, s10, 9
	s_add_i32 s6, s6, 69680
	v_add_u32_e32 v8, s6, v112
	ds_read_b128 v[0:3], v8
	ds_read_b128 v[4:7], v8 offset:16
	s_branch .Lq_done

	.amdhsa_kernel _Z11edge_kernelPK15HIP_vector_typeIjLj2EEPKiPiPS_IiLj2EEPKfPK6__halfPfSD_
		.amdhsa_group_segment_fixed_size 162864
		.amdhsa_private_segment_fixed_size 0
		.amdhsa_kernarg_size 64
		.amdhsa_user_sgpr_count 2
		.amdhsa_user_sgpr_dispatch_ptr 0
		.amdhsa_user_sgpr_queue_ptr 0
		.amdhsa_user_sgpr_kernarg_segment_ptr 1
		.amdhsa_user_sgpr_dispatch_id 0
		.amdhsa_user_sgpr_kernarg_preload_length 0
		.amdhsa_user_sgpr_kernarg_preload_offset 0
		.amdhsa_user_sgpr_private_segment_size 0
		.amdhsa_uses_dynamic_stack 0
		.amdhsa_enable_private_segment 0
		.amdhsa_system_sgpr_workgroup_id_x 1
		.amdhsa_system_sgpr_workgroup_id_y 0
		.amdhsa_system_sgpr_workgroup_id_z 0
		.amdhsa_system_sgpr_workgroup_info 0
		.amdhsa_system_vgpr_workitem_id 0
		.amdhsa_next_free_vgpr 128
		.amdhsa_next_free_sgpr 66
		.amdhsa_accum_offset 128
		.amdhsa_reserve_vcc 1
		.amdhsa_float_round_mode_32 0
		.amdhsa_float_round_mode_16_64 0
		.amdhsa_float_denorm_mode_32 3
		.amdhsa_float_denorm_mode_16_64 3
		.amdhsa_dx10_clamp 1
		.amdhsa_ieee_mode 1
		.amdhsa_fp16_overflow 0
		.amdhsa_tg_split 0
		.amdhsa_exception_fp_ieee_invalid_op 0
		.amdhsa_exception_fp_denorm_src 0
		.amdhsa_exception_fp_ieee_div_zero 0
		.amdhsa_exception_fp_ieee_overflow 0
		.amdhsa_exception_fp_ieee_underflow 0
		.amdhsa_exception_fp_ieee_inexact 0
		.amdhsa_exception_int_div_zero 0
	.end_amdhsa_kernel

amdhsa.kernels:
  - .agpr_count:     0
    .args:
      - .actual_access:  read_only
        .address_space:  global
        .offset:         0
        .size:           8
        .value_kind:     global_buffer
      - .actual_access:  read_only
        .address_space:  global
        .offset:         8
        .size:           8
        .value_kind:     global_buffer
      - .actual_access:  write_only
        .address_space:  global
        .offset:         16
        .size:           8
        .value_kind:     global_buffer
      - .actual_access:  write_only
        .address_space:  global
        .offset:         24
        .size:           8
        .value_kind:     global_buffer
      - .actual_access:  write_only
        .address_space:  global
        .offset:         32
        .size:           8
        .value_kind:     global_buffer
      - .actual_access:  read_only
        .address_space:  global
        .offset:         40
        .size:           8
        .value_kind:     global_buffer
      - .actual_access:  read_only
        .address_space:  global
        .offset:         48
        .size:           8
        .value_kind:     global_buffer
      - .actual_access:  read_only
        .address_space:  global
        .offset:         56
        .size:           8
        .value_kind:     global_buffer
      - .actual_access:  read_only
        .address_space:  global
        .offset:         64
        .size:           8
        .value_kind:     global_buffer
      - .actual_access:  write_only
        .address_space:  global
        .offset:         72
        .size:           8
        .value_kind:     global_buffer
      - .actual_access:  write_only
        .address_space:  global
        .offset:         80
        .size:           8
        .value_kind:     global_buffer
    .group_segment_fixed_size: 72704
    .kernarg_segment_align: 8
    .kernarg_segment_size: 88
    .language:       OpenCL C
    .language_version:
      - 2
      - 0
    .max_flat_workgroup_size: 512
    .name:           _Z9l1_kernelPKiS0_P15HIP_vector_typeIjLj2EEPiS4_PKfS6_S6_S6_PfP6__half
    .private_segment_fixed_size: 0
    .sgpr_count:     76
    .sgpr_spill_count: 0
    .symbol:         _Z9l1_kernelPKiS0_P15HIP_vector_typeIjLj2EEPiS4_PKfS6_S6_S6_PfP6__half.kd
    .uniform_work_group_size: 1
    .uses_dynamic_stack: false
    .vgpr_count:     252
    .vgpr_spill_count: 0
    .wavefront_size: 64
  - .agpr_count:     0
    .args:
      - .actual_access:  read_only
        .address_space:  global
        .offset:         0
        .size:           8
        .value_kind:     global_buffer
      - .actual_access:  read_only
        .address_space:  global
        .offset:         8
        .size:           8
        .value_kind:     global_buffer
      - .address_space:  global
        .offset:         16
        .size:           8
        .value_kind:     global_buffer
      - .address_space:  global
        .offset:         24
        .size:           8
        .value_kind:     global_buffer
      - .actual_access:  read_only
        .address_space:  global
        .offset:         32
        .size:           8
        .value_kind:     global_buffer
      - .actual_access:  read_only
        .address_space:  global
        .offset:         40
        .size:           8
        .value_kind:     global_buffer
      - .actual_access:  write_only
        .address_space:  global
        .offset:         48
        .size:           8
        .value_kind:     global_buffer
      - .actual_access:  write_only
        .address_space:  global
        .offset:         56
        .size:           8
        .value_kind:     global_buffer
    .group_segment_fixed_size: 162864
    .kernarg_segment_align: 8
    .kernarg_segment_size: 64
    .language:       OpenCL C
    .language_version:
      - 2
      - 0
    .max_flat_workgroup_size: 1024
    .name:           _Z11edge_kernelPK15HIP_vector_typeIjLj2EEPKiPiPS_IiLj2EEPKfPK6__halfPfSD_
    .private_segment_fixed_size: 0
    .sgpr_count:     72
    .sgpr_spill_count: 0
    .symbol:         _Z11edge_kernelPK15HIP_vector_typeIjLj2EEPKiPiPS_IiLj2EEPKfPK6__halfPfSD_.kd
    .uniform_work_group_size: 1
    .uses_dynamic_stack: false
    .vgpr_count:     128
    .vgpr_spill_count: 0
    .wavefront_size: 64
